# speedup vs baseline: 1.0178x; 1.0087x over previous
_Z9k_scatterPKiS0_PiPjPKfS4_S4_S4_PfS4_PDv4_j:
	s_load_dwordx4 s[4:7], s[0:1], 0x0
	s_mul_hi_i32 s9, s2, 0x30d4
	s_mul_i32 s8, s2, 0x30d4
	s_lshl_b64 s[24:25], s[8:9], 2
	v_or_b32_e32 v1, 0x400, v0
	s_waitcnt lgkmcnt(0)
	s_cmp_gt_u32 s2, 1
	s_cbranch_scc1 .Lk1_nopf
	s_load_dwordx8 s[36:43], s[0:1], 0x20
	s_load_dwordx2 s[44:45], s[0:1], 0x48
	v_cmp_gt_u32_e64 s[46:47], 64, v0
	s_and_saveexec_b64 s[48:49], s[46:47]
	v_lshlrev_b32_e32 v112, 6, v0
	s_waitcnt lgkmcnt(0)
	s_cmp_eq_u32 s2, 1
	s_cbranch_scc1 .Lk1_pfw1
	v_min_u32_e32 v108, 0x7c0, v112
	v_min_u32_e32 v109, 64, v112
	v_min_u32_e32 v110, 0xc0, v112
	v_mov_b32_e32 v111, 0
	global_load_dword v113, v108, s[36:37]
	global_load_dword v113, v109, s[38:39]
	global_load_dword v113, v110, s[40:41]
	global_load_dword v113, v111, s[42:43]
	s_branch .Lk1_pfend
.Lk1_pfw1:
	v_lshlrev_b32_e32 v108, 7, v0
	global_load_dword v113, v108, s[44:45]

.Lk1_nopf:
	s_add_u32 s6, s6, s24
	v_lshlrev_b32_e32 v45, 4, v1
	v_or_b32_e32 v1, 0x800, v0
	s_addc_u32 s7, s7, s25
	v_lshlrev_b32_e32 v44, 4, v0
	v_lshlrev_b32_e32 v47, 4, v1
	global_load_dwordx4 v[26:29], v44, s[6:7] nt
	global_load_dwordx4 v[18:21], v45, s[6:7] nt
	global_load_dwordx4 v[10:13], v47, s[6:7] nt
	v_or_b32_e32 v1, 0xc00, v0
	s_movk_i32 s3, 0xc35
	v_cmp_gt_u32_e32 vcc, s3, v1
	v_lshlrev_b32_e32 v46, 4, v1
	s_and_saveexec_b64 s[8:9], vcc
	s_cbranch_execz .LBB0_2
	global_load_dwordx4 v[2:5], v46, s[6:7] nt
